# attention: K fragment ds_reads issued before the LDS-DMA issue each tile
# speedup vs baseline: 1.0107x; 1.0107x over previous
.LBB0_538:
	s_add_i32 s78, s78, 1
	s_waitcnt lgkmcnt(4)
	s_waitcnt lgkmcnt(0)
	v_mfma_f32_32x32x16_bf16 v[96:111], v[80:83], v[124:127], v[0:15]
	s_add_i32 s79, s76, 1
	s_cmp_lg_u32 s76, 2
	s_cselect_b32 s76, s79, 0
	s_add_u32 s16, s16, 0xd8000
	s_addc_u32 s17, s17, 0
	s_add_u32 s54, s54, 0x30000
	s_addc_u32 s55, s55, 0
	v_mfma_f32_32x32x16_bf16 v[80:95], v[206:209], v[124:127], v[0:15]
	s_cmp_eq_u32 s78, 63
	v_mfma_f32_32x32x16_bf16 v[96:111], v[194:197], v[120:123], v[96:111]
	ds_read_b64_tr_b16 v[194:195], v193 offset:0
	ds_read_b64_tr_b16 v[196:197], v193 offset:512
	v_mfma_f32_32x32x16_bf16 v[80:95], v[210:213], v[120:123], v[80:95]
	v_mfma_f32_32x32x16_bf16 v[96:111], v[198:201], v[116:119], v[96:111]
	ds_read_b64_tr_b16 v[198:199], v193 offset:1024
	ds_read_b64_tr_b16 v[200:201], v193 offset:1536
	ds_read_b64_tr_b16 v[206:207], v193 offset:2048
	ds_read_b64_tr_b16 v[208:209], v193 offset:2560
	ds_read_b64_tr_b16 v[210:211], v193 offset:3072
	ds_read_b64_tr_b16 v[212:213], v193 offset:3584
	v_mfma_f32_32x32x16_bf16 v[80:95], v[214:217], v[116:119], v[80:95]
	v_mfma_f32_32x32x16_bf16 v[96:111], v[202:205], v[112:115], v[96:111]
	v_mfma_f32_32x32x16_bf16 v[80:95], v[218:221], v[112:115], v[80:95]
	s_nop 10
	v_exp_f32_e32 v222, v96
	v_exp_f32_e32 v223, v97
	v_exp_f32_e32 v224, v98
	v_exp_f32_e32 v225, v99
	v_exp_f32_e32 v226, v100
	v_exp_f32_e32 v227, v101
	v_exp_f32_e32 v228, v102
	v_exp_f32_e32 v229, v103
	v_exp_f32_e32 v218, v80
	v_exp_f32_e32 v219, v81
	ds_read_b64_tr_b16 v[80:81], v193 offset:4096
	v_exp_f32_e32 v220, v82
	v_exp_f32_e32 v221, v83
	ds_read_b64_tr_b16 v[82:83], v193 offset:4608
	v_exp_f32_e32 v234, v84
	v_exp_f32_e32 v235, v85
	ds_read_b64_tr_b16 v[84:85], v193 offset:5120
	v_cvt_pk_bf16_f32 v100, v222, v223
	v_cvt_pk_bf16_f32 v101, v224, v225
	v_cvt_pk_bf16_f32 v102, v226, v227
	v_cvt_pk_bf16_f32 v103, v228, v229
	v_exp_f32_e32 v236, v86
	v_exp_f32_e32 v237, v87
	ds_read_b64_tr_b16 v[86:87], v193 offset:5632
	v_exp_f32_e32 v230, v104
	v_exp_f32_e32 v214, v105
	ds_read_b64_tr_b16 v[104:105], v193 offset:6144
	v_exp_f32_e32 v215, v106
	v_exp_f32_e32 v216, v107
	ds_read_b64_tr_b16 v[106:107], v193 offset:6656
	v_exp_f32_e32 v217, v108
	v_exp_f32_e32 v231, v109
	ds_read_b64_tr_b16 v[108:109], v193 offset:7168
	v_exp_f32_e32 v232, v110
	v_exp_f32_e32 v233, v111
	ds_read_b64_tr_b16 v[110:111], v193 offset:7680
	s_waitcnt lgkmcnt(8)
	v_cvt_pk_bf16_f32 v96, v230, v214
	v_mfma_f32_32x32x16_bf16 v[64:79], v[100:103], v[194:197], v[64:79]
	v_cvt_pk_bf16_f32 v97, v215, v216
	v_cvt_pk_bf16_f32 v98, v217, v231
	v_cvt_pk_bf16_f32 v99, v232, v233
	ds_read_b64_tr_b16 v[194:195], v193 offset:8192
	v_exp_f32_e32 v238, v88
	v_exp_f32_e32 v239, v89
	v_exp_f32_e32 v240, v90
	v_mfma_f32_32x32x16_bf16 v[64:79], v[96:99], v[198:201], v[64:79]
	v_exp_f32_e32 v241, v91
	v_cvt_pk_bf16_f32 v88, v218, v219
	v_cvt_pk_bf16_f32 v89, v220, v221
	v_cvt_pk_bf16_f32 v90, v234, v235
	v_cvt_pk_bf16_f32 v91, v236, v237
	ds_read_b64_tr_b16 v[196:197], v193 offset:8704
	ds_read_b64_tr_b16 v[198:199], v193 offset:9216
	ds_read_b64_tr_b16 v[200:201], v193 offset:9728
	ds_read_b64_tr_b16 v[202:203], v193 offset:10240
	ds_read_b64_tr_b16 v[204:205], v193 offset:10752
	s_nop 1
	v_mfma_f32_32x32x16_bf16 v[64:79], v[88:91], v[206:209], v[64:79]
	ds_read_b64_tr_b16 v[206:207], v193 offset:11264
	ds_read_b64_tr_b16 v[208:209], v193 offset:11776
	s_waitcnt lgkmcnt(8)
	v_exp_f32_e32 v242, v92
	v_exp_f32_e32 v243, v93
	v_exp_f32_e32 v244, v94
	v_exp_f32_e32 v245, v95
	v_mfma_f32_32x32x16_bf16 v[48:63], v[100:103], v[80:83], v[48:63]
	ds_read_b64_tr_b16 v[80:81], v193 offset:12288
	v_cvt_pk_bf16_f32 v92, v238, v239
	v_cvt_pk_bf16_f32 v93, v240, v241
	v_cvt_pk_bf16_f32 v94, v242, v243
	v_cvt_pk_bf16_f32 v95, v244, v245
	ds_read_b64_tr_b16 v[82:83], v193 offset:12800
	v_mfma_f32_32x32x16_bf16 v[48:63], v[96:99], v[84:87], v[48:63]
	ds_read_b64_tr_b16 v[84:85], v193 offset:13312
	ds_read_b64_tr_b16 v[86:87], v193 offset:13824
	v_mfma_f32_32x32x16_bf16 v[48:63], v[88:91], v[104:107], v[48:63]
	ds_read_b64_tr_b16 v[104:105], v193 offset:14336
	ds_read_b64_tr_b16 v[106:107], v193 offset:14848
	v_mfma_f32_32x32x16_bf16 v[64:79], v[92:95], v[210:213], v[64:79]
	ds_read_b64_tr_b16 v[210:211], v193 offset:15360
	ds_read_b64_tr_b16 v[212:213], v193 offset:15872
	s_waitcnt lgkmcnt(8)
	s_nop 0
	s_waitcnt lgkmcnt(0)
	s_nop 0
	v_mfma_f32_32x32x16_bf16 v[16:31], v[100:103], v[80:83], v[16:31]
	v_add_f32_e32 v80, 0, v222
	v_add_f32_e32 v80, v223, v80
	v_add_f32_e32 v80, v224, v80
	v_add_f32_e32 v80, v225, v80
	v_add_f32_e32 v80, v226, v80
	v_add_f32_e32 v80, v227, v80
	v_add_f32_e32 v80, v228, v80
	v_mfma_f32_32x32x16_bf16 v[32:47], v[100:103], v[194:197], v[32:47]
	v_add_f32_e32 v80, v229, v80
	v_add_f32_e32 v80, v230, v80
	v_add_f32_e32 v80, v214, v80
	v_add_f32_e32 v80, v215, v80
	v_add_f32_e32 v80, v216, v80
	v_add_f32_e32 v80, v217, v80
	v_add_f32_e32 v80, v231, v80
	v_mfma_f32_32x32x16_bf16 v[16:31], v[96:99], v[84:87], v[16:31]
	v_add_f32_e32 v80, v232, v80
	v_add_f32_e32 v80, v233, v80
	v_add_f32_e32 v80, v218, v80
	v_add_f32_e32 v80, v219, v80
	v_add_f32_e32 v80, v220, v80
	v_add_f32_e32 v80, v221, v80
	v_add_f32_e32 v80, v234, v80
	v_mfma_f32_32x32x16_bf16 v[32:47], v[96:99], v[198:201], v[32:47]
	v_add_f32_e32 v80, v235, v80
	v_add_f32_e32 v80, v236, v80
	v_add_f32_e32 v80, v237, v80
	v_add_f32_e32 v80, v238, v80
	v_add_f32_e32 v80, v239, v80
	v_add_f32_e32 v80, v240, v80
	v_add_f32_e32 v80, v241, v80
	v_mfma_f32_32x32x16_bf16 v[16:31], v[88:91], v[104:107], v[16:31]
	v_add_f32_e32 v80, v242, v80
	v_add_f32_e32 v80, v243, v80
	v_add_f32_e32 v80, v244, v80
	v_add_f32_e32 v80, v245, v80
	v_add_f32_e32 v130, v130, v80
	v_mfma_f32_32x32x16_bf16 v[32:47], v[88:91], v[202:205], v[32:47]
	v_mfma_f32_32x32x16_bf16 v[48:63], v[92:95], v[108:111], v[48:63]
	v_mfma_f32_32x32x16_bf16 v[16:31], v[92:95], v[210:213], v[16:31]
	v_mfma_f32_32x32x16_bf16 v[32:47], v[92:95], v[206:209], v[32:47]
	s_cbranch_scc1 .LBB0_541
.LBB0_539:
	s_waitcnt vmcnt(5)
	s_waitcnt lgkmcnt(0)
	s_barrier
	s_mul_i32 s79, s77, 0x8800
	s_add_i32 s79, s64, s79
	s_add_i32 s80, s77, 1
	s_cmp_lg_u32 s77, 2
	s_cselect_b32 s77, s80, 0
	s_add_i32 s80, s79, s65
	v_add_u32_e32 v84, s80, v179
	ds_read_b128 v[80:83], v84 offset:0
	ds_read_b128 v[194:197], v84 offset:32
	ds_read_b128 v[198:201], v84 offset:64
	ds_read_b128 v[202:205], v84 offset:96
	ds_read_b128 v[206:209], v84 offset:4608
	ds_read_b128 v[210:213], v84 offset:4640
	ds_read_b128 v[214:217], v84 offset:4672
	ds_read_b128 v[218:221], v84 offset:4704
	s_addk_i32 s79, 0x4800
	v_add_u32_e32 v193, s79, v178
	s_cmp_gt_u32 s78, 61
	s_cbranch_scc1 .LBB0_538
	s_mul_i32 s79, s76, 0x8800
	s_and_b64 s[80:81], s[4:5], exec
	s_cselect_b32 s81, s55, s17
	s_cselect_b32 s80, s54, s16
	s_add_i32 s79, s79, s64
	v_lshl_add_u64 v[248:249], s[80:81], 0, v[168:169]
	s_add_i32 s80, s79, s45
	s_mov_b32 s81, m0
	s_mov_b32 m0, s80
	s_nop 0
	global_load_lds_dwordx4 v[248:249], off
	s_mov_b32 m0, s81
	s_and_b64 s[80:81], s[6:7], exec
	s_cselect_b32 s81, s55, s17
	s_cselect_b32 s80, s54, s16
	v_lshl_add_u64 v[248:249], s[80:81], 0, v[170:171]
	s_add_i32 s80, s79, s47
	s_mov_b32 s81, m0
	s_mov_b32 m0, s80
	s_nop 0
	global_load_lds_dwordx4 v[248:249], off
	s_mov_b32 m0, s81
	s_and_b64 s[80:81], s[8:9], exec
	s_cselect_b32 s81, s55, s17
	s_cselect_b32 s80, s54, s16
	v_lshl_add_u64 v[248:249], s[80:81], 0, v[172:173]
	s_add_i32 s80, s79, s49
	s_mov_b32 s81, m0
	s_mov_b32 m0, s80
	s_nop 0
	global_load_lds_dwordx4 v[248:249], off
	s_mov_b32 m0, s81
	s_and_b64 s[80:81], s[10:11], exec
	s_cselect_b32 s81, s55, s17
	s_cselect_b32 s80, s54, s16
	v_lshl_add_u64 v[248:249], s[80:81], 0, v[174:175]
	s_add_i32 s80, s79, s51
	s_mov_b32 s81, m0
	s_mov_b32 m0, s80
	s_nop 0
	global_load_lds_dwordx4 v[248:249], off
	s_mov_b32 m0, s81
	s_and_b64 s[80:81], s[12:13], exec
	s_cselect_b32 s81, s55, s17
	s_cselect_b32 s80, s54, s16
	v_lshl_add_u64 v[248:249], s[80:81], 0, v[176:177]
	s_add_i32 s79, s79, s53
	s_mov_b32 s80, m0
	s_mov_b32 m0, s79
	s_nop 0
	global_load_lds_dwordx4 v[248:249], off
	s_mov_b32 m0, s80
	s_branch .LBB0_538

	.amdhsa_kernel _Z10fwd_kernelILin1EEv4Args
		.amdhsa_group_segment_fixed_size 0
		.amdhsa_private_segment_fixed_size 0
		.amdhsa_kernarg_size 512
		.amdhsa_user_sgpr_count 2
		.amdhsa_user_sgpr_dispatch_ptr 0
		.amdhsa_user_sgpr_queue_ptr 0
		.amdhsa_user_sgpr_kernarg_segment_ptr 1
		.amdhsa_user_sgpr_dispatch_id 0
		.amdhsa_user_sgpr_kernarg_preload_length 0
		.amdhsa_user_sgpr_kernarg_preload_offset 0
		.amdhsa_user_sgpr_private_segment_size 0
		.amdhsa_uses_dynamic_stack 0
		.amdhsa_enable_private_segment 0
		.amdhsa_system_sgpr_workgroup_id_x 1
		.amdhsa_system_sgpr_workgroup_id_y 0
		.amdhsa_system_sgpr_workgroup_id_z 0
		.amdhsa_system_sgpr_workgroup_info 0
		.amdhsa_system_vgpr_workitem_id 0
		.amdhsa_next_free_vgpr 252
		.amdhsa_next_free_sgpr 98
		.amdhsa_accum_offset 252
		.amdhsa_reserve_vcc 1
		.amdhsa_float_round_mode_32 0
		.amdhsa_float_round_mode_16_64 0
		.amdhsa_float_denorm_mode_32 3
		.amdhsa_float_denorm_mode_16_64 3
		.amdhsa_dx10_clamp 1
		.amdhsa_ieee_mode 1
		.amdhsa_fp16_overflow 0
		.amdhsa_tg_split 0
		.amdhsa_exception_fp_ieee_invalid_op 0
		.amdhsa_exception_fp_denorm_src 0
		.amdhsa_exception_fp_ieee_div_zero 0
		.amdhsa_exception_fp_ieee_overflow 0
		.amdhsa_exception_fp_ieee_underflow 0
		.amdhsa_exception_fp_ieee_inexact 0
		.amdhsa_exception_int_div_zero 0
	.end_amdhsa_kernel

amdhsa.kernels:
  - .agpr_count:     0
    .args:
      - .offset:         0
        .size:           256
        .value_kind:     by_value
      - .offset:         256
        .size:           4
        .value_kind:     hidden_block_count_x
      - .offset:         260
        .size:           4
        .value_kind:     hidden_block_count_y
      - .offset:         264
        .size:           4
        .value_kind:     hidden_block_count_z
      - .offset:         268
        .size:           2
        .value_kind:     hidden_group_size_x
      - .offset:         270
        .size:           2
        .value_kind:     hidden_group_size_y
      - .offset:         272
        .size:           2
        .value_kind:     hidden_group_size_z
      - .offset:         274
        .size:           2
        .value_kind:     hidden_remainder_x
      - .offset:         276
        .size:           2
        .value_kind:     hidden_remainder_y
      - .offset:         278
        .size:           2
        .value_kind:     hidden_remainder_z
      - .offset:         296
        .size:           8
        .value_kind:     hidden_global_offset_x
      - .offset:         304
        .size:           8
        .value_kind:     hidden_global_offset_y
      - .offset:         312
        .size:           8
        .value_kind:     hidden_global_offset_z
      - .offset:         320
        .size:           2
        .value_kind:     hidden_grid_dims
      - .offset:         376
        .size:           4
        .value_kind:     hidden_dynamic_lds_size
    .group_segment_fixed_size: 0
    .kernarg_segment_align: 8
    .kernarg_segment_size: 512
    .language:       OpenCL C
    .language_version:
      - 2
      - 0
    .max_flat_workgroup_size: 512
    .name:           _Z10fwd_kernelILin1EEv4Args
    .private_segment_fixed_size: 0
    .sgpr_count:     104
    .sgpr_spill_count: 2
    .symbol:         _Z10fwd_kernelILin1EEv4Args.kd
    .uniform_work_group_size: 1
    .uses_dynamic_stack: false
    .vgpr_count:     252
    .vgpr_spill_count: 0
    .wavefront_size: 64
